# attention tile A: softmax row-sum as 14 v_pk_add_f32 on aligned pairs + 3 scalar adds (was 32 scalar adds); f32 accumulation, summation order changed
# baseline (speedup 1.0000x reference)
.LBB0_3238:
	v_pk_add_f32 v[16:17], v[146:147], v[148:149]
	v_pk_add_f32 v[16:17], v[16:17], v[150:151]
	v_pk_add_f32 v[16:17], v[16:17], v[152:153]
	v_pk_add_f32 v[16:17], v[16:17], v[154:155]
	v_pk_add_f32 v[16:17], v[16:17], v[156:157]
	v_pk_add_f32 v[16:17], v[16:17], v[158:159]
	v_pk_add_f32 v[16:17], v[16:17], v[160:161]
	v_exp_f32_e32 v2, v144
	v_exp_f32_e32 v4, v145
	v_exp_f32_e32 v5, v140
	v_exp_f32_e32 v6, v141
	v_exp_f32_e32 v7, v138
	v_exp_f32_e32 v8, v139
	v_exp_f32_e32 v9, v132
	v_exp_f32_e32 v10, v133
	v_exp_f32_e32 v11, v130
	v_exp_f32_e32 v12, v131
	v_exp_f32_e32 v13, v142
	v_exp_f32_e32 v14, v143
	v_exp_f32_e32 v15, v136
	v_exp_f32_e32 v19, v137
	v_exp_f32_e32 v32, v134
	v_exp_f32_e32 v33, v135
	v_pk_add_f32 v[16:17], v[16:17], v[4:5]
	v_pk_add_f32 v[16:17], v[16:17], v[6:7]
	v_pk_add_f32 v[16:17], v[16:17], v[8:9]
	v_pk_add_f32 v[16:17], v[16:17], v[10:11]
	v_pk_add_f32 v[16:17], v[16:17], v[12:13]
	v_pk_add_f32 v[16:17], v[16:17], v[14:15]
	v_pk_add_f32 v[16:17], v[16:17], v[32:33]
	v_add_f32_e32 v16, v16, v17
	v_add_f32_e32 v16, v2, v16
	v_add_f32_e32 v16, v19, v16
	v_mov_b32_e32 v17, v16
	v_cvt_pk_bf16_f32 v20, v154, v158
	v_cvt_pk_bf16_f32 v21, v155, v159
	v_cvt_pk_bf16_f32 v22, v156, v160
	v_cvt_pk_bf16_f32 v23, v157, v161
	v_cvt_pk_bf16_f32 v24, v146, v150
	v_cvt_pk_bf16_f32 v25, v147, v151
	v_cvt_pk_bf16_f32 v26, v148, v152
	v_cvt_pk_bf16_f32 v27, v149, v153
	v_cvt_pk_bf16_f32 v28, v2, v4
	v_cvt_pk_bf16_f32 v29, v5, v6
	v_cvt_pk_bf16_f32 v30, v7, v8
	v_cvt_pk_bf16_f32 v31, v9, v10
	v_cvt_pk_bf16_f32 v130, v11, v12
	v_cvt_pk_bf16_f32 v131, v13, v14
	v_cvt_pk_bf16_f32 v132, v15, v19
	v_cvt_pk_bf16_f32 v133, v32, v33
	s_add_i32 s2, s73, 2
	s_nop 0
	v_permlane32_swap_b32_e32 v16, v17
	v_permlane32_swap_b32_e32 v20, v22
	v_permlane32_swap_b32_e32 v21, v23
	v_permlane32_swap_b32_e32 v24, v26
	v_permlane32_swap_b32_e32 v25, v27
	v_permlane32_swap_b32_e32 v28, v30
	v_permlane32_swap_b32_e32 v29, v31
	v_permlane32_swap_b32_e32 v130, v132
	v_permlane32_swap_b32_e32 v131, v133
	s_and_b32 s12, s2, 0x7ffffffc
	s_lshr_b32 s92, s78, s12
	s_lshl_b32 s12, s92, 8
	s_and_b32 s12, s12, 0xf00
	s_and_b32 s94, s72, 0xc0
	s_or_b32 s12, s12, s94
	v_or_b32_e32 v2, s12, v227
	v_or_b32_e32 v6, s12, v1
	v_mul_u32_u24_e32 v2, 0x1800, v2
	v_mul_u32_u24_e32 v6, 0x1800, v6
	v_lshlrev_b32_e32 v2, 1, v2
	v_lshlrev_b32_e32 v12, 1, v6
	v_mov_b32_e32 v13, v3
	v_lshl_add_u64 v[4:5], v[192:193], 0, v[2:3]
	v_lshl_add_u64 v[8:9], v[192:193], 0, v[12:13]
	v_lshl_add_u64 v[14:15], v[194:195], 0, v[2:3]
	global_load_dwordx4 v[4:7], v[4:5], off
	s_nop 0
	global_load_dwordx4 v[8:11], v[8:9], off
	v_lshl_add_u64 v[32:33], v[194:195], 0, v[12:13]
	global_load_dwordx4 v[12:15], v[14:15], off
	s_nop 0
	global_load_dwordx4 v[178:181], v[32:33], off
	s_and_b32 s12, s73, -4
	s_lshr_b32 s12, s78, s12
	s_and_b32 s16, s12, 15
	s_cmp_lg_u32 s16, s80
	s_mov_b64 s[14:15], -1
	s_cbranch_scc0 .LBB0_3243
	s_lshr_b32 s12, s83, s16
	s_bitcmp1_b32 s12, 0
	s_cselect_b64 s[12:13], -1, 0
	s_cbranch_execz .LBB0_3244
